# attention main loop (7.2 wait at first consumer): the compiler's vmcnt(0) in front of the per-tile barrier removed, so the V prefetch stays in flight across the barrier (K DMA still covered by the des
# speedup vs baseline: 1.0003x; 1.0003x over previous
; #define VWRITE(b) do { *(LAS bf16x8*)(V_lds + (b) * SHM_V + vst0) = vs0; *(LAS bf16x8*)(V_lds + (b) * SHM_V + vst1) = vs1; } while (0)
; #define KWAIT_BAR(nv) do { if ((nv) == 2) asm volatile("s_waitcnt vmcnt(2)" ::: "memory"); else asm volatile("s_waitcnt vmcnt(0)" ::: "memory"); __syncthreads(); } while (0)
; #define SWAIT() asm volatile("s_waitcnt vmcnt(0)" ::: "memory")
; __device__ __forceinline__ void attn_unit(const bf16* __restrict__ Qraw, const float* __restrict__ ssq, const float* __restrict__ qn, int t0, const bf16* __restrict__ Kh, const bf16* __restrict__ Vh, bf16* __restrict__ Ob, int seq, LAS char* lds, int tid) {
;     ...
;         KWAIT_BAR(2);
;         SWAIT(); VWRITE(0); DMA_K((h + 2) * KVBLK, 1);
.LBB0_1466:
	s_add_u32 s10, s2, s60
	s_waitcnt vmcnt(2)
	s_barrier
	s_waitcnt vmcnt(0)
	ds_write_b128 v198, v[98:101]
	ds_write_b128 v199, v[102:105]
	v_mov_b32_e32 v146, v192
	v_mov_b32_e32 v98, v194
	v_mov_b32_e32 v100, v193
	s_addc_u32 s11, s3, s59
	v_mov_b32_e32 v101, v147
	v_lshl_add_u64 v[102:103], s[10:11], 0, v[146:147]
	s_mov_b32 m0, s36
	v_lshl_add_u64 v[102:103], v[102:103], 0, s[28:29]
	v_lshl_add_u64 v[100:101], s[10:11], 0, v[100:101]
	v_mov_b32_e32 v99, v147
	global_load_lds_dwordx4 v[102:103], off
	v_lshl_add_u64 v[100:101], v[100:101], 0, s[28:29]
	s_add_i32 m0, s36, 0x2000
	v_lshl_add_u64 v[98:99], s[10:11], 0, v[98:99]
	global_load_lds_dwordx4 v[100:101], off
	v_lshl_add_u64 v[98:99], v[98:99], 0, s[28:29]
	s_add_i32 m0, s36, 0x4000
	s_and_b64 vcc, exec, s[42:43]
	global_load_lds_dwordx4 v[98:99], off
	s_cbranch_vccnz .LBB0_1468
	s_add_u32 s10, s2, s60
	v_mov_b32_e32 v146, v196
	s_addc_u32 s11, s3, s59
	s_add_i32 m0, s36, 0x6000
	v_lshl_add_u64 v[98:99], s[10:11], 0, v[146:147]
	v_lshl_add_u64 v[98:99], v[98:99], 0, s[28:29]
	global_load_lds_dwordx4 v[98:99], off

; #define KWAIT_BAR(nv) do { if ((nv) == 2) asm volatile("s_waitcnt vmcnt(2)" ::: "memory"); else asm volatile("s_waitcnt vmcnt(0)" ::: "memory"); __syncthreads(); } while (0)
; __device__ __forceinline__ void partialSM(f32x16& p0, f32x16& p1, f32x16& negm, float& l_reg, f32x16* o, LAS float* al_l, int r32, int hi) {
;     ...
; #pragma unroll
;     for (int r = 0; r < 16; ++r) p0[r] = __builtin_amdgcn_exp2f(p0[r]);
; }
; __device__ __forceinline__ void attn_unit(const bf16* __restrict__ Qraw, const float* __restrict__ ssq, const float* __restrict__ qn, int t0, const bf16* __restrict__ Kh, const bf16* __restrict__ Vh, bf16* __restrict__ Ob, int seq, LAS char* lds, int tid) {
;     ...
;         KWAIT_BAR(2);
;     }
.LBB0_1470:
	v_exp_f32_e32 v228, v130
	v_exp_f32_e32 v231, v131
	v_exp_f32_e32 v229, v132
	v_exp_f32_e32 v232, v133
	v_exp_f32_e32 v230, v134
	v_exp_f32_e32 v233, v135
	v_exp_f32_e32 v226, v136
	v_exp_f32_e32 v227, v137
	v_exp_f32_e32 v204, v138
	v_exp_f32_e32 v206, v139
	v_exp_f32_e32 v205, v140
	v_exp_f32_e32 v207, v141
	v_exp_f32_e32 v184, v142
	v_exp_f32_e32 v202, v143
	v_exp_f32_e32 v185, v144
	v_exp_f32_e32 v203, v145
	s_waitcnt vmcnt(2)
	s_add_u32 s60, s60, 0xc000
	s_addc_u32 s59, s59, 0
	s_add_i32 s65, s65, 2
	s_cmp_ge_u32 s65, s57
	v_lshl_add_u64 v[182:183], v[182:183], 0, s[16:17]
	s_barrier
	s_cbranch_scc0 .LBB0_1462
	s_branch .LBB0_1477
